# batch loads for the next step issued before MFMA group 2 of the current step (LDS temps renamed off the batch register sets), on top of exact vmcnt counts
# speedup vs baseline: 1.0181x; 1.0181x over previous
.LBB1_6:
	s_lshr_b32 s57, s46, 2
	s_lshl_b32 s5, s46, 3
	s_lshl_b32 s4, s47, 3
	s_lshr_b32 s60, s47, 2
	s_add_i32 s59, s57, s51
	s_and_b64 s[4:5], s[4:5], s[38:39]
	s_add_i32 s58, s60, s45
	s_lshl_b32 s59, s59, 5
	v_or_b32_e32 v71, s5, v1
	s_lshl_b32 s58, s58, 5
	v_or_b32_e32 v72, s4, v68
	v_or_b32_e32 v71, s59, v71
	v_or_b32_e32 v72, s58, v72
	v_subrev_u32_e32 v74, s52, v71
	v_subrev_u32_e32 v73, s50, v72
	v_cmp_gt_i32_e32 vcc, s54, v74
	v_add_u32_e32 v75, 0xc8, v74
	v_add_u32_e32 v76, 0xc8, v73
	v_cndmask_b32_e64 v74, 0, 1, vcc
	v_cmp_gt_i32_e32 vcc, s49, v73
	v_cmp_gt_i32_e64 s[4:5], s53, v75
	s_cmp_lt_u32 s57, s55
	v_cndmask_b32_e64 v73, 0, 1, vcc
	v_cmp_gt_i32_e32 vcc, s48, v76
	s_cselect_b64 s[58:59], -1, 0
	s_cmp_lt_u32 s60, s42
	v_cndmask_b32_e64 v76, 0, 1, vcc
	v_cmp_gt_i32_e32 vcc, s50, v72
	v_cndmask_b32_e64 v72, 0, 1, s[4:5]
	v_cmp_gt_i32_e64 s[4:5], s52, v71
	s_cselect_b64 s[60:61], -1, 0
	s_lshl_b32 s62, 1, s46
	v_cndmask_b32_e64 v71, v74, v72, s[4:5]
	v_cndmask_b32_e32 v72, v73, v76, vcc
	v_and_b32_e32 v71, 1, v71
	v_and_b32_e32 v72, 1, v72
	v_cmp_eq_u32_e32 vcc, 1, v71
	s_lshl_b32 s57, 1, s47
	v_mov_b32_e32 v75, s62
	v_cmp_eq_u32_e64 s[4:5], 1, v72
	s_and_b64 vcc, s[58:59], vcc
	v_mov_b32_e32 v77, s57
	v_cndmask_b32_e32 v71, 0, v75, vcc
	s_and_b64 vcc, s[60:61], s[4:5]
	s_add_i32 s47, s47, 2
	s_add_i32 s46, s46, 2
	s_add_i32 s56, s56, -2
	v_cndmask_b32_e32 v72, 0, v77, vcc
	v_or_b32_e32 v70, v71, v70
	s_cmp_lg_u32 s56, 0
	v_or_b32_e32 v69, v72, v69
	s_cbranch_scc1 .LBB1_6
	v_lshrrev_b32_e32 v1, 1, v212
	v_xor_b32_e32 v72, v1, v68
	v_and_b32_e32 v196, 1, v0
	v_bitop3_b32 v1, v1, v68, 8 bitop3:0x1e
	v_lshlrev_b32_e32 v71, 9, v68
	v_lshlrev_b32_e32 v73, 3, v196
	v_lshlrev_b32_e32 v1, 4, v1
	v_or3_b32 v201, v1, v71, v73
	v_lshrrev_b32_e32 v1, 5, v212
	v_lshlrev_b32_e32 v72, 4, v72
	v_and_b32_e32 v68, 0x100, v0
	v_bitop3_b32 v74, v1, v0, 15 bitop3:0x78
	v_and_b32_e32 v214, 31, v0
	v_lshl_or_b32 v204, v214, 9, v68
	v_lshlrev_b32_e32 v203, 4, v74
	v_or3_b32 v202, v72, v71, v73
	v_or_b32_e32 v205, v69, v70
	s_waitcnt vmcnt(23)
	v_cvt_pk_f16_f32 v68, v62, v63
	v_cvt_pk_f16_f32 v69, v64, v65
	ds_write_b64 v202, v[68:69]
	v_and_b32_e32 v68, 1, v205
	v_cmp_eq_u32_e32 vcc, 0, v68
	s_mov_b32 s39, 0
	s_movk_i32 s45, 0x2000
	v_cndmask_b32_e64 v68, 1.0, 0, vcc
	v_pk_fma_f32 v[62:63], v[68:69], v[62:63], 0 op_sel_hi:[0,1,0]
	v_pk_fma_f32 v[64:65], v[68:69], v[64:65], 0 op_sel_hi:[0,1,0]
	s_waitcnt vmcnt(21)
	v_cvt_pk_f16_f32 v68, v58, v59
	v_cvt_pk_f16_f32 v69, v60, v61
	ds_write_b64 v201, v[68:69] offset:4096
	v_and_b32_e32 v68, 2, v205
	v_cmp_eq_u32_e32 vcc, 0, v68
	s_nop 1
	v_cndmask_b32_e64 v68, 1.0, 0, vcc
	v_pk_fma_f32 v[58:59], v[68:69], v[58:59], v[62:63] op_sel_hi:[0,1,1]
	s_waitcnt vmcnt(19)
	v_cvt_pk_f16_f32 v62, v54, v55
	v_cvt_pk_f16_f32 v63, v56, v57
	ds_write_b64 v202, v[62:63] offset:8192
	v_and_b32_e32 v62, 4, v205
	v_cmp_eq_u32_e32 vcc, 0, v62
	v_pk_fma_f32 v[60:61], v[68:69], v[60:61], v[64:65] op_sel_hi:[0,1,1]
	s_nop 0
	v_cndmask_b32_e64 v62, 1.0, 0, vcc
	v_pk_fma_f32 v[54:55], v[62:63], v[54:55], v[58:59] op_sel_hi:[0,1,1]
	s_waitcnt vmcnt(17)
	v_cvt_pk_f16_f32 v58, v50, v51
	v_cvt_pk_f16_f32 v59, v52, v53
	ds_write_b64 v201, v[58:59] offset:12288
	v_and_b32_e32 v58, 8, v205
	v_cmp_eq_u32_e32 vcc, 0, v58
	v_pk_fma_f32 v[56:57], v[62:63], v[56:57], v[60:61] op_sel_hi:[0,1,1]
	s_nop 0
	v_cndmask_b32_e64 v58, 1.0, 0, vcc
	v_pk_fma_f32 v[50:51], v[58:59], v[50:51], v[54:55] op_sel_hi:[0,1,1]
	v_pk_fma_f32 v[52:53], v[58:59], v[52:53], v[56:57] op_sel_hi:[0,1,1]
	v_cvt_pk_f16_f32 v50, v50, v51
	v_cvt_pk_f16_f32 v51, v52, v53
	v_or_b32_e32 v52, 0x20000, v202
	ds_write_b64 v52, v[50:51]
	v_cvt_pk_f16_f32 v50, v46, v47
	v_cvt_pk_f16_f32 v51, v48, v49
	ds_write_b64 v202, v[50:51] offset:16384
	v_and_b32_e32 v50, 16, v205
	v_cmp_eq_u32_e32 vcc, 0, v50
	s_nop 1
	v_cndmask_b32_e64 v50, 1.0, 0, vcc
	v_pk_fma_f32 v[46:47], v[50:51], v[46:47], 0 op_sel_hi:[0,1,0]
	v_pk_fma_f32 v[48:49], v[50:51], v[48:49], 0 op_sel_hi:[0,1,0]
	v_cvt_pk_f16_f32 v50, v42, v43
	v_cvt_pk_f16_f32 v51, v44, v45
	ds_write_b64 v201, v[50:51] offset:20480
	v_and_b32_e32 v50, 32, v205
	v_cmp_eq_u32_e32 vcc, 0, v50
	s_nop 1
	v_cndmask_b32_e64 v50, 1.0, 0, vcc
	v_pk_fma_f32 v[42:43], v[50:51], v[42:43], v[46:47] op_sel_hi:[0,1,1]
	v_cvt_pk_f16_f32 v46, v38, v39
	v_cvt_pk_f16_f32 v47, v40, v41
	ds_write_b64 v202, v[46:47] offset:24576
	v_and_b32_e32 v46, 64, v205
	v_cmp_eq_u32_e32 vcc, 0, v46
	v_pk_fma_f32 v[44:45], v[50:51], v[44:45], v[48:49] op_sel_hi:[0,1,1]
	s_nop 0
	v_cndmask_b32_e64 v46, 1.0, 0, vcc
	v_pk_fma_f32 v[38:39], v[46:47], v[38:39], v[42:43] op_sel_hi:[0,1,1]
	s_waitcnt vmcnt(16)
	v_cvt_pk_f16_f32 v42, v34, v35
	v_cvt_pk_f16_f32 v43, v36, v37
	ds_write_b64 v201, v[42:43] offset:28672
	v_and_b32_e32 v42, 0x80, v205
	v_cmp_eq_u32_e32 vcc, 0, v42
	v_pk_fma_f32 v[40:41], v[46:47], v[40:41], v[44:45] op_sel_hi:[0,1,1]
	s_nop 0
	v_cndmask_b32_e64 v42, 1.0, 0, vcc
	v_pk_fma_f32 v[34:35], v[42:43], v[34:35], v[38:39] op_sel_hi:[0,1,1]
	v_pk_fma_f32 v[36:37], v[42:43], v[36:37], v[40:41] op_sel_hi:[0,1,1]
	v_cvt_pk_f16_f32 v34, v34, v35
	v_cvt_pk_f16_f32 v35, v36, v37
	v_or_b32_e32 v36, 0x21000, v201
	ds_write_b64 v36, v[34:35]
	s_waitcnt vmcnt(15)
	v_cvt_pk_f16_f32 v34, v30, v31
	v_cvt_pk_f16_f32 v35, v32, v33
	ds_write_b64 v202, v[34:35] offset:32768
	v_and_b32_e32 v34, 0x100, v205
	v_cmp_eq_u32_e32 vcc, 0, v34
	s_waitcnt vmcnt(13)
	v_cvt_pk_f16_f32 v34, v26, v27
	v_cvt_pk_f16_f32 v35, v28, v29
	ds_write_b64 v201, v[34:35] offset:36864
	v_and_b32_e32 v34, 0x200, v205
	v_cndmask_b32_e64 v186, 1.0, 0, vcc
	v_cmp_eq_u32_e32 vcc, 0, v34
	v_mov_b32_e32 v187, v186
	v_pk_fma_f32 v[30:31], v[186:187], v[30:31], 0 op_sel_hi:[0,1,0]
	v_cndmask_b32_e64 v188, 1.0, 0, vcc
	v_mov_b32_e32 v189, v188
	v_pk_fma_f32 v[26:27], v[188:189], v[26:27], v[30:31] op_sel_hi:[0,1,1]
	s_waitcnt vmcnt(11)
	v_cvt_pk_f16_f32 v30, v22, v23
	v_cvt_pk_f16_f32 v31, v24, v25
	ds_write_b64 v202, v[30:31] offset:40960
	v_and_b32_e32 v30, 0x400, v205
	v_cmp_eq_u32_e32 vcc, 0, v30
	v_pk_fma_f32 v[32:33], v[186:187], v[32:33], 0 op_sel_hi:[0,1,0]
	v_pk_fma_f32 v[28:29], v[188:189], v[28:29], v[32:33] op_sel_hi:[0,1,1]
	v_cndmask_b32_e64 v190, 1.0, 0, vcc
	v_mov_b32_e32 v191, v190
	v_pk_fma_f32 v[22:23], v[190:191], v[22:23], v[26:27] op_sel_hi:[0,1,1]
	s_waitcnt vmcnt(9)
	v_cvt_pk_f16_f32 v26, v18, v19
	v_cvt_pk_f16_f32 v27, v20, v21
	ds_write_b64 v201, v[26:27] offset:45056
	v_and_b32_e32 v26, 0x800, v205
	v_cmp_eq_u32_e32 vcc, 0, v26
	v_pk_fma_f32 v[24:25], v[190:191], v[24:25], v[28:29] op_sel_hi:[0,1,1]
	s_nop 0
	v_cndmask_b32_e64 v192, 1.0, 0, vcc
	v_mov_b32_e32 v193, v192
	v_pk_fma_f32 v[18:19], v[192:193], v[18:19], v[22:23] op_sel_hi:[0,1,1]
	v_pk_fma_f32 v[20:21], v[192:193], v[20:21], v[24:25] op_sel_hi:[0,1,1]
	v_cvt_pk_f16_f32 v18, v18, v19
	v_cvt_pk_f16_f32 v19, v20, v21
	v_or_b32_e32 v20, 0x22000, v202
	ds_write_b64 v20, v[18:19]
	v_cvt_pk_f16_f32 v18, v14, v15
	v_cvt_pk_f16_f32 v19, v16, v17
	ds_write_b64 v202, v[18:19] offset:49152
	v_and_b32_e32 v18, 0x1000, v205
	v_cmp_eq_u32_e32 vcc, 0, v18
	v_cvt_pk_f16_f32 v18, v10, v11
	v_cvt_pk_f16_f32 v19, v12, v13
	ds_write_b64 v201, v[18:19] offset:53248
	v_and_b32_e32 v18, 0x2000, v205
	v_cndmask_b32_e64 v178, 1.0, 0, vcc
	v_cmp_eq_u32_e32 vcc, 0, v18
	v_mov_b32_e32 v179, v178
	v_pk_fma_f32 v[14:15], v[178:179], v[14:15], 0 op_sel_hi:[0,1,0]
	v_cndmask_b32_e64 v180, 1.0, 0, vcc
	v_mov_b32_e32 v181, v180
	v_pk_fma_f32 v[10:11], v[180:181], v[10:11], v[14:15] op_sel_hi:[0,1,1]
	v_cvt_pk_f16_f32 v14, v6, v7
	v_cvt_pk_f16_f32 v15, v8, v9
	ds_write_b64 v202, v[14:15] offset:57344
	v_and_b32_e32 v14, 0x4000, v205
	v_cmp_eq_u32_e32 vcc, 0, v14
	v_pk_fma_f32 v[16:17], v[178:179], v[16:17], 0 op_sel_hi:[0,1,0]
	v_pk_fma_f32 v[12:13], v[180:181], v[12:13], v[16:17] op_sel_hi:[0,1,1]
	v_cndmask_b32_e64 v182, 1.0, 0, vcc
	v_mov_b32_e32 v183, v182
	v_pk_fma_f32 v[6:7], v[182:183], v[6:7], v[10:11] op_sel_hi:[0,1,1]
	s_waitcnt vmcnt(8)
	v_cvt_pk_f16_f32 v10, v2, v3
	v_cvt_pk_f16_f32 v11, v4, v5
	ds_write_b64 v201, v[10:11] offset:61440
	v_and_b32_e32 v10, 0x8000, v205
	v_cmp_eq_u32_e32 vcc, 0, v10
	v_pk_fma_f32 v[8:9], v[182:183], v[8:9], v[12:13] op_sel_hi:[0,1,1]
	s_nop 0
	v_cndmask_b32_e64 v184, 1.0, 0, vcc
	v_mov_b32_e32 v185, v184
	v_pk_fma_f32 v[2:3], v[184:185], v[2:3], v[6:7] op_sel_hi:[0,1,1]
	v_pk_fma_f32 v[4:5], v[184:185], v[4:5], v[8:9] op_sel_hi:[0,1,1]
	v_cvt_pk_f16_f32 v2, v2, v3
	v_cvt_pk_f16_f32 v3, v4, v5
	v_or_b32_e32 v4, 0x23000, v201
	ds_write_b64 v4, v[2:3]
	v_mov_b32_e32 v2, 0
	s_add_i32 s46, s42, -1
	v_lshl_add_u64 v[194:195], s[40:41], 0, v[66:67]
	v_or_b32_e32 v206, 0x20000, v204
	s_mov_b32 s41, -3
	s_movk_i32 s40, 0x3000
	s_mov_b32 s4, s20
	s_mov_b32 s5, s21
	s_mov_b32 s20, 0
	v_mov_b32_e32 v3, v2
	v_mov_b32_e32 v4, v2
	v_mov_b32_e32 v5, v2
	v_mov_b32_e32 v6, v2
	v_mov_b32_e32 v7, v2
	v_mov_b32_e32 v8, v2
	v_mov_b32_e32 v9, v2
	v_mov_b32_e32 v10, v2
	v_mov_b32_e32 v11, v2
	v_mov_b32_e32 v12, v2
	v_mov_b32_e32 v13, v2
	v_mov_b32_e32 v14, v2
	v_mov_b32_e32 v15, v2
	v_mov_b32_e32 v16, v2
	v_mov_b32_e32 v17, v2
	v_mov_b32_e32 v34, v2
	v_mov_b32_e32 v35, v2
	v_mov_b32_e32 v36, v2
	v_mov_b32_e32 v37, v2
	v_mov_b32_e32 v38, v2
	v_mov_b32_e32 v39, v2
	v_mov_b32_e32 v40, v2
	v_mov_b32_e32 v41, v2
	v_mov_b32_e32 v42, v2
	v_mov_b32_e32 v43, v2
	v_mov_b32_e32 v44, v2
	v_mov_b32_e32 v45, v2
	v_mov_b32_e32 v46, v2
	v_mov_b32_e32 v47, v2
	v_mov_b32_e32 v48, v2
	v_mov_b32_e32 v49, v2
	v_mov_b32_e32 v50, v2
	v_mov_b32_e32 v51, v2
	v_mov_b32_e32 v52, v2
	v_mov_b32_e32 v53, v2
	v_mov_b32_e32 v54, v2
	v_mov_b32_e32 v55, v2
	v_mov_b32_e32 v56, v2
	v_mov_b32_e32 v57, v2
	v_mov_b32_e32 v58, v2
	v_mov_b32_e32 v59, v2
	v_mov_b32_e32 v60, v2
	v_mov_b32_e32 v61, v2
	v_mov_b32_e32 v62, v2
	v_mov_b32_e32 v63, v2
	v_mov_b32_e32 v64, v2
	v_mov_b32_e32 v65, v2
	v_mov_b32_e32 v18, v2
	v_mov_b32_e32 v19, v2
	v_mov_b32_e32 v20, v2
	v_mov_b32_e32 v21, v2
	v_mov_b32_e32 v22, v2
	v_mov_b32_e32 v23, v2
	v_mov_b32_e32 v24, v2
	v_mov_b32_e32 v25, v2
	v_mov_b32_e32 v26, v2
	v_mov_b32_e32 v27, v2
	v_mov_b32_e32 v28, v2
	v_mov_b32_e32 v29, v2
	v_mov_b32_e32 v30, v2
	v_mov_b32_e32 v31, v2
	v_mov_b32_e32 v32, v2
	v_mov_b32_e32 v33, v2
	v_mov_b32_e32 v66, v2
	v_mov_b32_e32 v67, v2
	v_mov_b32_e32 v68, v2
	v_mov_b32_e32 v69, v2
	v_mov_b32_e32 v70, v2
	v_mov_b32_e32 v71, v2
	v_mov_b32_e32 v72, v2
	v_mov_b32_e32 v73, v2
	v_mov_b32_e32 v74, v2
	v_mov_b32_e32 v75, v2
	v_mov_b32_e32 v76, v2
	v_mov_b32_e32 v77, v2
	v_mov_b32_e32 v78, v2
	v_mov_b32_e32 v79, v2
	v_mov_b32_e32 v80, v2
	v_mov_b32_e32 v81, v2
	s_add_i32 s75, s44, 1
	s_lshl_b32 s75, s75, 10
	s_and_b32 s75, s75, 0x1c00
	s_min_u32 s76, 2, s46
	s_lshl_b32 s76, s76, 18
	s_or_b32 s75, s75, s76
	s_mov_b32 s76, 0
	v_add_u32_e32 v154, s76, v197
	v_add_u32_e32 v155, s76, v198
	v_add_u32_e32 v156, s76, v199
	v_add_u32_e32 v157, s76, v200
	buffer_load_dwordx4 v[174:177], v154, s[4:7], s75 offen sc0 nt sc1
	buffer_load_dwordx4 v[170:173], v155, s[4:7], s75 offen sc0 nt sc1
	buffer_load_dwordx4 v[162:165], v156, s[4:7], s75 offen sc0 nt sc1
	buffer_load_dwordx4 v[154:157], v157, s[4:7], s75 offen sc0 nt sc1
	s_waitcnt lgkmcnt(0)
	s_barrier
.LBB1_8:
	s_add_i32 s50, s41, 5
	s_lshr_b32 s38, s50, 2
	s_add_i32 s38, s38, s44
	s_lshl_b32 s38, s38, 17
	s_add_i32 s47, s20, 0x8000
	s_add_i32 s48, s41, 9
	s_and_b32 s38, s38, 0xe0000
	s_and_b32 s47, s47, 0xc000
	s_lshr_b32 s49, s48, 2
	s_or_b32 s38, s38, s47
	s_and_b32 s47, s48, 3
	s_add_i32 s49, s49, s44
	v_lshl_add_u64 v[150:151], v[194:195], 0, s[38:39]
	s_min_u32 s38, s47, s46
	s_lshl_b32 s49, s49, 10
	s_and_b32 s49, s49, 0x1c00
	s_lshl_b32 s38, s38, 18
	s_add_i32 s21, s41, 3
	v_add_co_u32_e32 v146, vcc, s45, v150
	s_or_b32 s38, s49, s38
	s_nop 0
	v_addc_co_u32_e32 v147, vcc, 0, v151, vcc
	s_cmp_lt_u32 s21, 26
	v_add_co_u32_e32 v152, vcc, s40, v150
	s_cselect_b32 s49, 0, 2.0
	s_nop 0
	v_addc_co_u32_e32 v153, vcc, 0, v151, vcc
	global_load_dwordx4 v[158:161], v[146:147], off offset:-4096
	s_nop 0
	global_load_dwordx4 v[146:149], v[146:147], off
	s_nop 0
	global_load_dwordx4 v[166:169], v[150:151], off
	s_nop 0
	global_load_dwordx4 v[150:153], v[152:153], off
	s_nop 0
	s_nop 0
	s_and_b32 s51, s21, 3
	s_bfe_u32 s38, s21, 0x10002
	s_lshl_b32 s49, s51, 6
	v_lshl_or_b32 v207, s38, 16, v204
	v_xor_b32_e32 v215, s49, v203
	v_add_u32_e32 v226, v207, v215
	ds_read_b128 v[208:211], v226
	ds_read_b128 v[216:219], v226 offset:16384
	ds_read_b128 v[220:223], v226 offset:32768
	ds_read_b128 v[226:229], v226 offset:49152
	v_lshl_add_u32 v240, s38, 14, v206
	v_add_u32_e32 v230, v240, v215
	ds_read_b128 v[230:233], v230
	s_add_i32 s38, s20, 0x10000
	s_and_b32 s38, s38, 0x10000
	s_lshl_b32 s49, s51, 14
	s_or_b32 s38, s38, s49
	s_lshl_b32 s53, s51, 2
	s_cmp_lg_u32 s41, -3
	s_cbranch_scc1 .Lsteady_w1
	s_waitcnt vmcnt(9)
.Lsteady_w1:
	s_waitcnt vmcnt(19)
	v_cvt_pk_f16_f32 v234, v142, v143
	v_cvt_pk_f16_f32 v235, v144, v145
	v_or_b32_e32 v236, s38, v202
	ds_write_b64 v236, v[234:235]
	v_bfe_u32 v234, v205, s53, 1
	v_cmp_eq_u32_e32 vcc, 0, v234
	v_lshrrev_b32_e32 v241, s53, v205
	s_waitcnt vmcnt(18)
	v_cvt_pk_f16_f32 v236, v138, v139
	v_cndmask_b32_e64 v234, 1.0, 0, vcc
	v_pk_fma_f32 v[142:143], v[234:235], v[142:143], 0 op_sel_hi:[0,1,0]
	v_cvt_pk_f16_f32 v237, v140, v141
	v_or_b32_e32 v235, s38, v201
	ds_write_b64 v235, v[236:237] offset:4096
	v_and_b32_e32 v235, 2, v241
	v_cmp_eq_u32_e32 vcc, 0, v235
	s_add_i32 s52, s41, 7
	s_nop 0
	v_cndmask_b32_e64 v236, 1.0, 0, vcc
	v_pk_fma_f32 v[238:239], v[236:237], v[138:139], v[142:143] op_sel_hi:[0,1,1]
	v_xor_b32_e32 v215, 32, v215
	s_waitcnt lgkmcnt(6)
	v_mfma_f32_32x32x16_f16 v[2:17], v[118:121], v[208:211], v[2:17]
	v_add_u32_e32 v207, v207, v215
	v_fma_f32 v138, v234, v144, 0
	v_fma_f32 v139, v234, v145, 0
	s_waitcnt lgkmcnt(5)
	v_mfma_f32_32x32x16_f16 v[34:49], v[118:121], v[216:219], v[34:49]
	s_waitcnt lgkmcnt(4)
	v_mfma_f32_32x32x16_f16 v[50:65], v[118:121], v[220:223], v[50:65]
	v_fma_f32 v220, v236, v140, v138
	v_fma_f32 v221, v236, v141, v139
	v_add_u32_e32 v254, v240, v215
	s_waitcnt lgkmcnt(3)
	v_mfma_f32_32x32x16_f16 v[18:33], v[118:121], v[226:229], v[18:33]
	ds_read_b128 v[118:121], v207
	ds_read_b128 v[250:253], v207 offset:16384
	ds_read_b128 v[208:211], v207 offset:32768
	ds_read_b128 v[216:219], v207 offset:49152
	ds_read_b128 v[234:237], v254
	s_waitcnt lgkmcnt(7)
	v_mfma_f32_32x32x16_f16 v[66:81], v[114:117], v[230:233], v[66:81]
	s_bfe_u32 s38, s52, 0x10002
	s_lshl_b32 s53, s38, 16
	s_or_b32 s49, s53, s49
	s_waitcnt vmcnt(17)
	v_cvt_pk_f16_f32 v114, v134, v135
	v_cvt_pk_f16_f32 v115, v136, v137
	v_or_b32_e32 v116, s49, v202
	ds_write_b64 v116, v[114:115] offset:8192
	v_and_b32_e32 v114, 4, v241
	v_cmp_eq_u32_e32 vcc, 0, v114
	s_lshl_b32 s38, s38, 14
	s_nop 0
	v_cndmask_b32_e64 v114, 1.0, 0, vcc
	v_pk_fma_f32 v[116:117], v[114:115], v[134:135], v[238:239] op_sel_hi:[0,1,1]
	v_pk_fma_f32 v[114:115], v[114:115], v[136:137], v[220:221] op_sel_hi:[0,1,1]
	s_waitcnt vmcnt(16)
	v_cvt_pk_f16_f32 v134, v130, v131
	v_cvt_pk_f16_f32 v135, v132, v133
	v_or_b32_e32 v136, s49, v201
	s_lshl_b32 s49, s51, 12
	ds_write_b64 v136, v[134:135] offset:12288
	v_and_b32_e32 v134, 8, v241
	s_or_b32 s38, s38, s49
	v_cmp_eq_u32_e32 vcc, 0, v134
	s_bitcmp0_b32 s21, 0
	s_nop 0
	v_cndmask_b32_e64 v134, 1.0, 0, vcc
	s_cselect_b64 vcc, -1, 0
	v_pk_fma_f32 v[116:117], v[134:135], v[130:131], v[116:117] op_sel_hi:[0,1,1]
	v_pk_fma_f32 v[114:115], v[134:135], v[132:133], v[114:115] op_sel_hi:[0,1,1]
	v_cndmask_b32_e32 v207, v201, v202, vcc
	v_cvt_pk_f16_f32 v116, v116, v117
	v_cvt_pk_f16_f32 v117, v114, v115
	v_or_b32_e32 v114, s38, v207
	v_or_b32_e32 v114, 0x20000, v114
	ds_write_b64 v114, v[116:117]
	s_add_i32 s75, s21, 7
	s_and_b32 s76, s75, 3
	s_lshr_b32 s75, s75, 2
	s_add_i32 s75, s75, s44
	s_min_u32 s76, s76, s46
	s_lshl_b32 s75, s75, 10
	s_and_b32 s75, s75, 0x1c00
	s_lshl_b32 s76, s76, 18
	s_or_b32 s75, s75, s76
	s_cmp_lt_u32 s21, 25
	s_cselect_b32 s76, 0, 2.0
	v_add_u32_e32 v130, s76, v197
	v_add_u32_e32 v131, s76, v198
	v_add_u32_e32 v132, s76, v199
	v_add_u32_e32 v133, s76, v200
	buffer_load_dwordx4 v[142:145], v130, s[4:7], s75 offen sc0 nt sc1
	buffer_load_dwordx4 v[138:141], v131, s[4:7], s75 offen sc0 nt sc1
	buffer_load_dwordx4 v[134:137], v132, s[4:7], s75 offen sc0 nt sc1
	buffer_load_dwordx4 v[130:133], v133, s[4:7], s75 offen sc0 nt sc1
	s_waitcnt lgkmcnt(7)
	v_mfma_f32_32x32x16_f16 v[2:17], v[90:93], v[118:121], v[2:17]
	s_waitcnt lgkmcnt(6)
	v_mfma_f32_32x32x16_f16 v[34:49], v[90:93], v[250:253], v[34:49]
	s_waitcnt lgkmcnt(5)
	v_mfma_f32_32x32x16_f16 v[50:65], v[90:93], v[208:211], v[50:65]
	s_waitcnt lgkmcnt(4)
	v_mfma_f32_32x32x16_f16 v[18:33], v[90:93], v[216:219], v[18:33]
	s_waitcnt lgkmcnt(3)
	v_mfma_f32_32x32x16_f16 v[66:81], v[98:101], v[234:237], v[66:81]
	s_cmp_lg_u32 s51, 3
	s_cbranch_scc1 .LBB1_10
	s_waitcnt lgkmcnt(0)
	s_barrier
.LBB1_10:
	s_add_i32 s38, s41, 6
	s_lshr_b32 s38, s38, 2
	s_add_i32 s38, s38, s44
	s_lshl_b32 s38, s38, 17
	s_add_i32 s49, s20, 0xc000
	s_and_b32 s38, s38, 0xe0000
	s_and_b32 s53, s49, 0xc000
	s_or_b32 s38, s38, s53
	v_lshl_add_u64 v[90:91], v[194:195], 0, s[38:39]
	s_add_i32 s38, s41, 10
	s_and_b32 s53, s38, 3
	s_lshr_b32 s38, s38, 2
	s_add_i32 s38, s38, s44
	v_add_co_u32_e32 v92, vcc, 0x1000, v90
	s_min_u32 s53, s53, s46
	s_lshl_b32 s38, s38, 10
	v_addc_co_u32_e32 v93, vcc, 0, v91, vcc
	s_and_b32 s38, s38, 0x1c00
	s_lshl_b32 s53, s53, 18
	global_load_dwordx4 v[118:121], v[90:91], off
	global_load_dwordx4 v[114:117], v[92:93], off
	v_add_co_u32_e32 v92, vcc, 0x2000, v90
	s_or_b32 s38, s38, s53
	s_nop 0
	v_addc_co_u32_e32 v93, vcc, 0, v91, vcc
	s_cmp_lt_u32 s21, 25
	v_add_co_u32_e32 v98, vcc, 0x3000, v90
	s_cselect_b32 s53, 0, 2.0
	s_nop 0
	v_addc_co_u32_e32 v99, vcc, 0, v91, vcc
	global_load_dwordx4 v[90:93], v[92:93], off
	s_nop 0
	global_load_dwordx4 v[98:101], v[98:99], off
	s_nop 0
	s_nop 0
	s_add_i32 s38, s41, 4
	s_bfe_u32 s53, s38, 0x10002
	s_and_b32 s38, s38, 3
	s_lshl_b32 s54, s38, 6
	v_lshl_or_b32 v215, s53, 16, v204
	v_xor_b32_e32 v240, s54, v203
	v_add_u32_e32 v226, v215, v240
	ds_read_b128 v[208:211], v226
	ds_read_b128 v[216:219], v226 offset:16384
	ds_read_b128 v[220:223], v226 offset:32768
	ds_read_b128 v[226:229], v226 offset:49152
	v_lshl_add_u32 v241, s53, 14, v206
	v_add_u32_e32 v230, v241, v240
	ds_read_b128 v[230:233], v230
	s_add_i32 s53, s41, 8
	s_and_b32 s54, s53, 3
	s_add_i32 s55, s20, 0x14000
	s_and_b32 s55, s55, 0x10000
	s_lshl_b32 s56, s54, 14
	s_or_b32 s55, s55, s56
	s_lshl_b32 s57, s54, 2
	s_waitcnt vmcnt(19)
	v_cvt_pk_f16_f32 v234, v126, v127
	v_cvt_pk_f16_f32 v235, v128, v129
	v_or_b32_e32 v236, s55, v202
	ds_write_b64 v236, v[234:235]
	v_bfe_u32 v234, v205, s57, 1
	v_cmp_eq_u32_e32 vcc, 0, v234
	v_lshrrev_b32_e32 v242, s57, v205
	s_waitcnt vmcnt(18)
	v_cvt_pk_f16_f32 v236, v122, v123
	v_cndmask_b32_e64 v234, 1.0, 0, vcc
	v_pk_fma_f32 v[126:127], v[234:235], v[126:127], 0 op_sel_hi:[0,1,0]
	v_cvt_pk_f16_f32 v237, v124, v125
	v_or_b32_e32 v235, s55, v201
	ds_write_b64 v235, v[236:237] offset:4096
	v_and_b32_e32 v235, 2, v242
	v_cmp_eq_u32_e32 vcc, 0, v235
	s_nop 1
	v_cndmask_b32_e64 v236, 1.0, 0, vcc
	v_pk_fma_f32 v[238:239], v[236:237], v[122:123], v[126:127] op_sel_hi:[0,1,1]
	s_waitcnt lgkmcnt(4)
	v_mfma_f32_32x32x16_f16 v[50:65], v[102:105], v[220:223], v[50:65]
	v_xor_b32_e32 v222, 32, v240
	v_add_u32_e32 v215, v215, v222
	v_fma_f32 v122, v234, v128, 0
	v_fma_f32 v123, v234, v129, 0
	v_fma_f32 v220, v236, v124, v122
	v_fma_f32 v221, v236, v125, v123
	v_add_u32_e32 v254, v241, v222
	v_mfma_f32_32x32x16_f16 v[2:17], v[102:105], v[208:211], v[2:17]
	v_mfma_f32_32x32x16_f16 v[34:49], v[102:105], v[216:219], v[34:49]
	s_waitcnt lgkmcnt(3)
	v_mfma_f32_32x32x16_f16 v[18:33], v[102:105], v[226:229], v[18:33]
	ds_read_b128 v[102:105], v215
	ds_read_b128 v[250:253], v215 offset:16384
	ds_read_b128 v[208:211], v215 offset:32768
	ds_read_b128 v[216:219], v215 offset:49152
	ds_read_b128 v[234:237], v254
	s_waitcnt lgkmcnt(7)
	v_mfma_f32_32x32x16_f16 v[66:81], v[94:97], v[230:233], v[66:81]
	s_bfe_u32 s55, s53, 0x10002
	s_lshl_b32 s57, s55, 16
	s_or_b32 s56, s57, s56
	s_waitcnt vmcnt(17)
	v_cvt_pk_f16_f32 v94, v110, v111
	v_cvt_pk_f16_f32 v95, v112, v113
	v_or_b32_e32 v96, s56, v202
	ds_write_b64 v96, v[94:95] offset:8192
	v_and_b32_e32 v94, 4, v242
	v_cmp_eq_u32_e32 vcc, 0, v94
	s_lshl_b32 s55, s55, 14
	s_lshl_b32 s54, s54, 12
	v_cndmask_b32_e64 v94, 1.0, 0, vcc
	v_pk_fma_f32 v[96:97], v[94:95], v[110:111], v[238:239] op_sel_hi:[0,1,1]
	v_pk_fma_f32 v[94:95], v[94:95], v[112:113], v[220:221] op_sel_hi:[0,1,1]
	s_waitcnt vmcnt(16)
	v_cvt_pk_f16_f32 v110, v106, v107
	v_cvt_pk_f16_f32 v111, v108, v109
	v_or_b32_e32 v112, s56, v201
	ds_write_b64 v112, v[110:111] offset:12288
	v_and_b32_e32 v110, 8, v242
	v_cmp_eq_u32_e32 vcc, 0, v110
	s_or_b32 s54, s55, s54
	s_bitcmp0_b32 s53, 0
	v_cndmask_b32_e64 v110, 1.0, 0, vcc
	v_pk_fma_f32 v[96:97], v[110:111], v[106:107], v[96:97] op_sel_hi:[0,1,1]
	v_pk_fma_f32 v[94:95], v[110:111], v[108:109], v[94:95] op_sel_hi:[0,1,1]
	s_cselect_b64 vcc, -1, 0
	v_cvt_pk_f16_f32 v96, v96, v97
	v_cvt_pk_f16_f32 v97, v94, v95
	v_cndmask_b32_e32 v94, v201, v202, vcc
	v_or_b32_e32 v94, s54, v94
	v_or_b32_e32 v94, 0x20000, v94
	ds_write_b64 v94, v[96:97]
	s_add_i32 s75, s21, 8
	s_and_b32 s76, s75, 3
	s_lshr_b32 s75, s75, 2
	s_add_i32 s75, s75, s44
	s_min_u32 s76, s76, s46
	s_lshl_b32 s75, s75, 10
	s_and_b32 s75, s75, 0x1c00
	s_lshl_b32 s76, s76, 18
	s_or_b32 s75, s75, s76
	s_cmp_lt_u32 s21, 24
	s_cselect_b32 s76, 0, 2.0
	v_add_u32_e32 v106, s76, v197
	v_add_u32_e32 v107, s76, v198
	v_add_u32_e32 v108, s76, v199
	v_add_u32_e32 v109, s76, v200
	buffer_load_dwordx4 v[126:129], v106, s[4:7], s75 offen sc0 nt sc1
	buffer_load_dwordx4 v[122:125], v107, s[4:7], s75 offen sc0 nt sc1
	buffer_load_dwordx4 v[110:113], v108, s[4:7], s75 offen sc0 nt sc1
	buffer_load_dwordx4 v[106:109], v109, s[4:7], s75 offen sc0 nt sc1
	s_waitcnt lgkmcnt(7)
	v_mfma_f32_32x32x16_f16 v[2:17], v[82:85], v[102:105], v[2:17]
	s_waitcnt lgkmcnt(6)
	v_mfma_f32_32x32x16_f16 v[34:49], v[82:85], v[250:253], v[34:49]
	s_waitcnt lgkmcnt(5)
	v_mfma_f32_32x32x16_f16 v[50:65], v[82:85], v[208:211], v[50:65]
	s_waitcnt lgkmcnt(4)
	v_mfma_f32_32x32x16_f16 v[18:33], v[82:85], v[216:219], v[18:33]
	s_waitcnt lgkmcnt(3)
	v_mfma_f32_32x32x16_f16 v[66:81], v[86:89], v[234:237], v[66:81]
	s_cmp_lg_u32 s38, 3
	s_cbranch_scc1 .LBB1_12
	s_waitcnt lgkmcnt(0)
	s_barrier
.LBB1_12:
	s_lshr_b32 s38, s52, 2
	s_add_i32 s38, s38, s44
	s_lshl_b32 s38, s38, 17
	s_and_b32 s38, s38, 0xe0000
	s_and_b32 s52, s20, 0xc000
	s_or_b32 s38, s38, s52
	v_lshl_add_u64 v[82:83], v[194:195], 0, s[38:39]
	s_add_i32 s38, s41, 11
	s_lshr_b32 s38, s38, 2
	s_add_i32 s38, s38, s44
	v_add_co_u32_e32 v84, vcc, 0x1000, v82
	s_min_u32 s41, s51, s46
	s_lshl_b32 s38, s38, 10
	v_addc_co_u32_e32 v85, vcc, 0, v83, vcc
	s_and_b32 s38, s38, 0x1c00
	s_lshl_b32 s41, s41, 18
	global_load_dwordx4 v[102:105], v[82:83], off
	global_load_dwordx4 v[94:97], v[84:85], off
	v_add_co_u32_e32 v84, vcc, 0x2000, v82
	s_or_b32 s38, s38, s41
	s_nop 0
	v_addc_co_u32_e32 v85, vcc, 0, v83, vcc
	s_cmp_lt_u32 s21, 24
	v_add_co_u32_e32 v86, vcc, 0x3000, v82
	s_cselect_b32 s41, 0, 2.0
	s_nop 0
	v_addc_co_u32_e32 v87, vcc, 0, v83, vcc
	global_load_dwordx4 v[82:85], v[84:85], off
	s_nop 0
	global_load_dwordx4 v[86:89], v[86:87], off
	s_nop 0
	s_nop 0
	s_and_b32 s41, s50, 3
	s_bfe_u32 s38, s50, 0x10002
	s_lshl_b32 s50, s41, 6
	v_lshl_or_b32 v215, s38, 16, v204
	v_xor_b32_e32 v240, s50, v203
	v_add_u32_e32 v226, v215, v240
	ds_read_b128 v[208:211], v226
	ds_read_b128 v[216:219], v226 offset:16384
	ds_read_b128 v[220:223], v226 offset:32768
	ds_read_b128 v[226:229], v226 offset:49152
	v_lshl_add_u32 v241, s38, 14, v206
	v_add_u32_e32 v230, v241, v240
	ds_read_b128 v[230:233], v230
	s_add_i32 s20, s20, 0x18000
	s_and_b32 s20, s20, 0x10000
	s_lshl_b32 s38, s47, 14
	s_or_b32 s20, s20, s38
	s_lshl_b32 s50, s47, 2
	s_waitcnt vmcnt(19)
	v_cvt_pk_f16_f32 v234, v174, v175
	v_cvt_pk_f16_f32 v235, v176, v177
	v_or_b32_e32 v236, s20, v202
	ds_write_b64 v236, v[234:235]
	v_bfe_u32 v234, v205, s50, 1
	v_cmp_eq_u32_e32 vcc, 0, v234
	v_lshrrev_b32_e32 v242, s50, v205
	s_waitcnt vmcnt(17)
	v_cvt_pk_f16_f32 v236, v170, v171
	v_cndmask_b32_e64 v234, 1.0, 0, vcc
	v_pk_fma_f32 v[174:175], v[234:235], v[174:175], 0 op_sel_hi:[0,1,0]
	v_cvt_pk_f16_f32 v237, v172, v173
	v_or_b32_e32 v235, s20, v201
	ds_write_b64 v235, v[236:237] offset:4096
	v_and_b32_e32 v235, 2, v242
	v_cmp_eq_u32_e32 vcc, 0, v235
	s_nop 1
	v_cndmask_b32_e64 v236, 1.0, 0, vcc
	v_pk_fma_f32 v[238:239], v[236:237], v[170:171], v[174:175] op_sel_hi:[0,1,1]
	s_waitcnt lgkmcnt(4)
	v_mfma_f32_32x32x16_f16 v[50:65], v[166:169], v[220:223], v[50:65]
	v_xor_b32_e32 v222, 32, v240
	v_add_u32_e32 v215, v215, v222
	v_fma_f32 v170, v234, v176, 0
	v_fma_f32 v171, v234, v177, 0
	v_fma_f32 v220, v236, v172, v170
	v_fma_f32 v221, v236, v173, v171
	v_add_u32_e32 v254, v241, v222
	v_mfma_f32_32x32x16_f16 v[2:17], v[166:169], v[208:211], v[2:17]
	v_mfma_f32_32x32x16_f16 v[34:49], v[166:169], v[216:219], v[34:49]
	s_waitcnt lgkmcnt(3)
	v_mfma_f32_32x32x16_f16 v[18:33], v[166:169], v[226:229], v[18:33]
	ds_read_b128 v[166:169], v215
	ds_read_b128 v[250:253], v215 offset:16384
	ds_read_b128 v[208:211], v215 offset:32768
	ds_read_b128 v[216:219], v215 offset:49152
	ds_read_b128 v[234:237], v254
	s_waitcnt lgkmcnt(7)
	v_mfma_f32_32x32x16_f16 v[66:81], v[158:161], v[230:233], v[66:81]
	s_bfe_u32 s20, s48, 0x10002
	s_lshl_b32 s48, s20, 16
	s_or_b32 s38, s48, s38
	s_waitcnt vmcnt(17)
	v_cvt_pk_f16_f32 v158, v162, v163
	v_cvt_pk_f16_f32 v159, v164, v165
	v_or_b32_e32 v160, s38, v202
	ds_write_b64 v160, v[158:159] offset:8192
	v_and_b32_e32 v158, 4, v242
	v_cmp_eq_u32_e32 vcc, 0, v158
	s_lshl_b32 s20, s20, 14
	s_nop 0
	v_cndmask_b32_e64 v158, 1.0, 0, vcc
	v_pk_fma_f32 v[160:161], v[158:159], v[162:163], v[238:239] op_sel_hi:[0,1,1]
	v_pk_fma_f32 v[158:159], v[158:159], v[164:165], v[220:221] op_sel_hi:[0,1,1]
	s_waitcnt vmcnt(16)
	v_cvt_pk_f16_f32 v162, v154, v155
	v_cvt_pk_f16_f32 v163, v156, v157
	v_or_b32_e32 v164, s38, v201
	ds_write_b64 v164, v[162:163] offset:12288
	v_and_b32_e32 v162, 8, v242
	v_cmp_eq_u32_e32 vcc, 0, v162
	s_lshl_b32 s38, s47, 12
	s_or_b32 s20, s20, s38
	v_cndmask_b32_e64 v162, 1.0, 0, vcc
	v_pk_fma_f32 v[154:155], v[162:163], v[154:155], v[160:161] op_sel_hi:[0,1,1]
	v_pk_fma_f32 v[156:157], v[162:163], v[156:157], v[158:159] op_sel_hi:[0,1,1]
	v_cvt_pk_f16_f32 v154, v154, v155
	v_cvt_pk_f16_f32 v155, v156, v157
	v_or_b32_e32 v156, s20, v207
	v_or_b32_e32 v156, 0x20000, v156
	ds_write_b64 v156, v[154:155]
	s_cmp_gt_u32 s21, 26
	s_cbranch_scc1 .Lskip_c
	s_add_i32 s75, s21, 9
	s_and_b32 s76, s75, 3
	s_lshr_b32 s75, s75, 2
	s_add_i32 s75, s75, s44
	s_min_u32 s76, s76, s46
	s_lshl_b32 s75, s75, 10
	s_and_b32 s75, s75, 0x1c00
	s_lshl_b32 s76, s76, 18
	s_or_b32 s75, s75, s76
	s_cmp_lt_u32 s21, 23
	s_cselect_b32 s76, 0, 2.0
	v_add_u32_e32 v154, s76, v197
	v_add_u32_e32 v155, s76, v198
	v_add_u32_e32 v156, s76, v199
	v_add_u32_e32 v157, s76, v200
	buffer_load_dwordx4 v[174:177], v154, s[4:7], s75 offen sc0 nt sc1
	buffer_load_dwordx4 v[170:173], v155, s[4:7], s75 offen sc0 nt sc1
	buffer_load_dwordx4 v[162:165], v156, s[4:7], s75 offen sc0 nt sc1
	buffer_load_dwordx4 v[154:157], v157, s[4:7], s75 offen sc0 nt sc1
.Lskip_c:
	s_waitcnt lgkmcnt(7)
	v_mfma_f32_32x32x16_f16 v[2:17], v[146:149], v[166:169], v[2:17]
	s_waitcnt lgkmcnt(6)
	v_mfma_f32_32x32x16_f16 v[34:49], v[146:149], v[250:253], v[34:49]
	s_waitcnt lgkmcnt(5)
	v_mfma_f32_32x32x16_f16 v[50:65], v[146:149], v[208:211], v[50:65]
	s_waitcnt lgkmcnt(4)
	v_mfma_f32_32x32x16_f16 v[18:33], v[146:149], v[216:219], v[18:33]
	s_waitcnt lgkmcnt(3)
	v_mfma_f32_32x32x16_f16 v[66:81], v[150:153], v[234:237], v[66:81]
	s_cmp_lg_u32 s41, 3
	s_cbranch_scc1 .LBB1_14
	s_waitcnt lgkmcnt(0)
	s_barrier

amdhsa.kernels:
  - .agpr_count:     0
    .args:
      - .actual_access:  read_only
        .address_space:  global
        .offset:         0
        .size:           8
        .value_kind:     global_buffer
      - .actual_access:  read_only
        .address_space:  global
        .offset:         8
        .size:           8
        .value_kind:     global_buffer
      - .actual_access:  read_only
        .address_space:  global
        .offset:         16
        .size:           8
        .value_kind:     global_buffer
      - .actual_access:  read_only
        .address_space:  global
        .offset:         24
        .size:           8
        .value_kind:     global_buffer
      - .actual_access:  read_only
        .address_space:  global
        .offset:         32
        .size:           8
        .value_kind:     global_buffer
      - .actual_access:  read_only
        .address_space:  global
        .offset:         40
        .size:           8
        .value_kind:     global_buffer
      - .actual_access:  read_only
        .address_space:  global
        .offset:         48
        .size:           8
        .value_kind:     global_buffer
      - .actual_access:  read_only
        .address_space:  global
        .offset:         56
        .size:           8
        .value_kind:     global_buffer
      - .actual_access:  write_only
        .address_space:  global
        .offset:         64
        .size:           8
        .value_kind:     global_buffer
      - .actual_access:  write_only
        .address_space:  global
        .offset:         72
        .size:           8
        .value_kind:     global_buffer
      - .actual_access:  write_only
        .address_space:  global
        .offset:         80
        .size:           8
        .value_kind:     global_buffer
      - .actual_access:  write_only
        .address_space:  global
        .offset:         88
        .size:           8
        .value_kind:     global_buffer
    .group_segment_fixed_size: 512
    .kernarg_segment_align: 8
    .kernarg_segment_size: 96
    .language:       OpenCL C
    .language_version:
      - 2
      - 0
    .max_flat_workgroup_size: 256
    .name:           _Z11prep_kernelPKfS0_S0_S0_S0_S0_S0_S0_PDF16_PfS2_Pj
    .private_segment_fixed_size: 0
    .sgpr_count:     18
    .sgpr_spill_count: 0
    .symbol:         _Z11prep_kernelPKfS0_S0_S0_S0_S0_S0_S0_PDF16_PfS2_Pj.kd
    .uniform_work_group_size: 1
    .uses_dynamic_stack: false
    .vgpr_count:     67
    .vgpr_spill_count: 0
    .wavefront_size: 64
  - .agpr_count:     0
    .args:
      - .actual_access:  read_only
        .address_space:  global
        .offset:         0
        .size:           8
        .value_kind:     global_buffer
      - .actual_access:  read_only
        .address_space:  global
        .offset:         8
        .size:           8
        .value_kind:     global_buffer
      - .actual_access:  read_only
        .address_space:  global
        .offset:         16
        .size:           8
        .value_kind:     global_buffer
      - .address_space:  global
        .offset:         24
        .size:           8
        .value_kind:     global_buffer
      - .address_space:  global
        .offset:         32
        .size:           8
        .value_kind:     global_buffer
      - .actual_access:  read_only
        .address_space:  global
        .offset:         40
        .size:           8
        .value_kind:     global_buffer
      - .actual_access:  read_only
        .address_space:  global
        .offset:         48
        .size:           8
        .value_kind:     global_buffer
      - .actual_access:  read_only
        .address_space:  global
        .offset:         56
        .size:           8
        .value_kind:     global_buffer
      - .actual_access:  read_only
        .address_space:  global
        .offset:         64
        .size:           8
        .value_kind:     global_buffer
      - .actual_access:  read_only
        .address_space:  global
        .offset:         72
        .size:           8
        .value_kind:     global_buffer
      - .actual_access:  read_only
        .address_space:  global
        .offset:         80
        .size:           8
        .value_kind:     global_buffer
      - .actual_access:  read_only
        .address_space:  global
        .offset:         88
        .size:           8
        .value_kind:     global_buffer
      - .actual_access:  read_only
        .address_space:  global
        .offset:         96
        .size:           8
        .value_kind:     global_buffer
      - .actual_access:  read_only
        .address_space:  global
        .offset:         104
        .size:           8
        .value_kind:     global_buffer
      - .actual_access:  read_only
        .address_space:  global
        .offset:         112
        .size:           8
        .value_kind:     global_buffer
      - .actual_access:  read_only
        .address_space:  global
        .offset:         120
        .size:           8
        .value_kind:     global_buffer
      - .actual_access:  write_only
        .address_space:  global
        .offset:         128
        .size:           8
        .value_kind:     global_buffer
    .group_segment_fixed_size: 163840
    .kernarg_segment_align: 8
    .kernarg_segment_size: 136
    .language:       OpenCL C
    .language_version:
      - 2
      - 0
    .max_flat_workgroup_size: 512
    .name:           _Z12fused_kernelPKfPKiPKDF16_PfPjS0_S0_S0_S0_S0_S0_S0_S0_S0_S0_S0_S5_
    .private_segment_fixed_size: 0
    .sgpr_count:     83
    .sgpr_spill_count: 0
    .symbol:         _Z12fused_kernelPKfPKiPKDF16_PfPjS0_S0_S0_S0_S0_S0_S0_S0_S0_S0_S0_S5_.kd
    .uniform_work_group_size: 1
    .uses_dynamic_stack: false
    .vgpr_count:     256
    .vgpr_spill_count: 0
    .wavefront_size: 64
